# speedup vs baseline: 1.0010x; 1.0010x over previous
.LBB2_116:
	s_waitcnt vmcnt(0)
	v_and_b32_e32 v115, 15, v110
	v_lshlrev_b32_e32 v122, 4, v110
	v_mov_b32_e32 v23, 0
	v_mov_b32_e32 v123, v23
	v_or_b32_e32 v0, s33, v115
	v_lshl_add_u64 v[20:21], s[16:17], 0, v[122:123]
	s_mov_b32 s0, 0x4d000
	v_ashrrev_i32_e32 v1, 31, v0
	v_add_co_u32_e32 v36, vcc, s0, v20
	v_lshlrev_b64 v[0:1], 7, v[0:1]
	s_nop 0
	v_addc_co_u32_e32 v37, vcc, 0, v21, vcc
	s_mov_b32 s0, 0x4c000
	v_lshl_add_u64 v[4:5], s[28:29], 0, v[0:1]
	v_lshlrev_b32_e32 v22, 3, v107
	v_add_co_u32_e32 v54, vcc, s0, v20
	v_lshl_add_u64 v[12:13], v[4:5], 0, v[22:23]
	s_nop 0
	v_addc_co_u32_e32 v55, vcc, 0, v21, vcc
	global_load_dwordx2 v[4:5], v[12:13], off
	global_load_dwordx2 v[6:7], v[12:13], off offset:32
	global_load_dwordx2 v[24:25], v[12:13], off offset:64
	global_load_dwordx2 v[26:27], v[12:13], off offset:96
	global_load_dwordx4 v[146:149], v[36:37], off
	global_load_dwordx4 v[138:141], v[54:55], off offset:2048
	global_load_dwordx4 v[130:133], v[36:37], off offset:-4096
	global_load_dwordx4 v[154:157], v[36:37], off offset:2048
	global_load_dwordx4 v[134:137], v[54:55], off offset:1024
	global_load_dwordx4 v[142:145], v[54:55], off offset:3072
	global_load_dwordx4 v[150:153], v[36:37], off offset:1024
	global_load_dwordx4 v[158:161], v[36:37], off offset:3072
	v_lshlrev_b32_e32 v22, 4, v107
	v_lshlrev_b32_e32 v244, 4, v110
	v_mov_b32_e32 v245, 0
	s_mov_b32 s92, 0x4e000
	s_mov_b32 s93, 0
	v_lshl_add_u64 v[244:245], s[16:17], 0, v[244:245]
	s_mov_b32 s94, 0x1000
	s_mov_b32 s95, 0
	v_lshl_add_u64 v[244:245], v[244:245], 0, s[92:93]
	v_lshl_add_u64 v[246:247], v[244:245], 0, s[94:95]
	global_load_dwordx4 v[164:167], v22, s[18:19]
	global_load_dwordx4 v[200:203], v22, s[18:19] offset:64
	global_load_dwordx4 v[204:207], v22, s[18:19] offset:128
	global_load_dwordx4 v[208:211], v22, s[18:19] offset:192
	global_load_dwordx4 v[184:187], v22, s[14:15]
	global_load_dwordx4 v[188:191], v22, s[14:15] offset:64
	global_load_dwordx4 v[192:195], v22, s[14:15] offset:128
	global_load_dwordx4 v[196:199], v22, s[14:15] offset:192
	global_load_dwordx4 v[212:215], v[244:245], off
	global_load_dwordx4 v[216:219], v[244:245], off offset:1024
	global_load_dwordx4 v[220:223], v[244:245], off offset:2048
	global_load_dwordx4 v[224:227], v[244:245], off offset:3072
	global_load_dwordx4 v[228:231], v[246:247], off
	global_load_dwordx4 v[232:235], v[246:247], off offset:1024
	global_load_dwordx4 v[236:239], v[246:247], off offset:2048
	global_load_dwordx4 v[240:243], v[246:247], off offset:3072
	s_mov_b32 s0, 0x3f200000
	s_waitcnt vmcnt(23)
	v_mfma_f32_16x16x32_f16 v[28:31], v[146:149], v[4:7], v[42:45]
	s_waitcnt vmcnt(22)
	v_mfma_f32_16x16x32_f16 v[16:19], v[138:141], v[4:7], v[46:49]
	s_waitcnt vmcnt(21)
	v_mfma_f32_16x16x32_f16 v[0:3], v[130:133], v[4:7], v[50:53]
	s_waitcnt vmcnt(20)
	v_mfma_f32_16x16x32_f16 v[32:35], v[154:157], v[4:7], v[38:41]
	s_waitcnt vmcnt(19)
	s_nop 1
	v_mfma_f32_16x16x32_f16 v[12:15], v[134:137], v[24:27], v[0:3]
	s_waitcnt vmcnt(18)
	v_mfma_f32_16x16x32_f16 v[8:11], v[142:145], v[24:27], v[16:19]
	s_waitcnt vmcnt(17)
	v_mfma_f32_16x16x32_f16 v[4:7], v[150:153], v[24:27], v[28:31]
	s_waitcnt vmcnt(16)
	v_mfma_f32_16x16x32_f16 v[0:3], v[158:161], v[24:27], v[32:35]
	s_waitcnt vmcnt(0)
	v_mov_b64_e32 v[16:17], v[164:165]
	v_mov_b64_e32 v[18:19], v[166:167]
	v_add_f32_e32 v24, v12, v16
	v_cmp_nlt_f32_e64 s[0:1], |v24|, s0
	s_and_saveexec_b64 s[2:3], s[0:1]
	s_xor_b64 s[0:1], exec, s[2:3]
	s_cbranch_execz .LBB2_118
	v_add_f32_e64 v12, |v24|, |v24|
	v_mul_f32_e32 v16, 0x3fb8aa3b, v12
	s_mov_b32 s2, 0x3fb8aa3b
	v_rndne_f32_e32 v25, v16
	v_sub_f32_e32 v26, v16, v25
	v_fma_f32 v16, v12, s2, -v16
	v_fmamk_f32 v16, v12, 0x32a5705f, v16
	v_add_f32_e32 v16, v26, v16
	v_exp_f32_e32 v16, v16
	v_cvt_i32_f32_e32 v25, v25
	s_mov_b32 s2, 0xc2ce8ed0
	v_cmp_ngt_f32_e32 vcc, s2, v12
	s_mov_b32 s2, 0x42b17218
	v_ldexp_f32 v16, v16, v25
	v_cndmask_b32_e32 v16, 0, v16, vcc
	v_mov_b32_e32 v25, 0x7f800000
	v_cmp_nlt_f32_e32 vcc, s2, v12
	s_nop 1
	v_cndmask_b32_e32 v12, v25, v16, vcc
	v_add_f32_e32 v12, 1.0, v12
	v_rcp_f32_e32 v12, v12
	s_nop 0
	v_fma_f32 v25, v12, -2.0, 1.0
